# U1: six wave-uniform mask negations (v_cndmask 0/1 + v_cmp_ne pair) replaced by one s_andn2_b64 each (attention V phase, gemm/out-proj headers); on top of A8 stack
# baseline (speedup 1.0000x reference)
.LBB0_545:
	s_waitcnt vmcnt(16)
	ds_read_b128 v[60:63], v78 offset:32800
	s_waitcnt vmcnt(7)
	s_andn2_b64 s[4:5], exec, s[14:15]
	s_andn2_b64 vcc, exec, s[14:15]
	s_mov_b64 s[16:17], -1
	s_cbranch_vccnz .LBB0_547
	s_waitcnt vmcnt(6) lgkmcnt(0)
	v_mfma_f32_32x32x16_bf16 v[16:31], v[60:63], v[56:59], v[0:15]
	s_cbranch_execnz .LBB0_549
	s_branch .LBB0_548

.LBB0_715:
	s_or_b64 exec, exec, s[10:11]
	s_andn2_b64 s[10:11], exec, s[14:15]
	s_andn2_b64 vcc, exec, s[14:15]
	s_mov_b64 s[14:15], -1
	s_cbranch_vccnz .LBB0_719
	v_add_u32_e32 v0, s34, v158
	ds_read_b32 v0, v0
	s_add_i32 s49, s48, 1
	s_mov_b32 s50, 0
	s_waitcnt lgkmcnt(0)
	v_cndmask_b32_e64 v0, v0, -1, s[8:9]
	v_cndmask_b32_e64 v1, v0, v204, s[4:5]
	v_mov_b32_e32 v0, 0

.LBB0_842:
	s_and_saveexec_b64 s[0:1], s[14:15]
	v_mov_b32_e32 v47, v82
	v_mov_b64_e32 v[0:1], v[32:33]
	v_mov_b64_e32 v[2:3], v[34:35]
	v_mov_b64_e32 v[4:5], v[36:37]
	v_mov_b64_e32 v[6:7], v[38:39]
	v_mov_b64_e32 v[8:9], v[40:41]
	v_mov_b64_e32 v[10:11], v[42:43]
	v_mov_b64_e32 v[12:13], v[44:45]
	v_mov_b64_e32 v[14:15], v[46:47]
	s_or_b64 exec, exec, s[0:1]
	v_max_f32_e32 v16, v65, v65
	v_max_f32_e32 v17, v64, v64
	v_max_f32_e32 v16, v17, v16
	v_max3_f32 v16, v16, v66, v67
	v_max3_f32 v16, v16, v68, v69
	v_max3_f32 v16, v16, v70, v71
	v_max3_f32 v16, v16, v72, v73
	v_max3_f32 v16, v16, v74, v75
	v_max3_f32 v16, v16, v76, v77
	v_max3_f32 v16, v16, v78, v79
	v_max3_f32 v16, v16, v0, v1
	v_max3_f32 v16, v16, v2, v3
	v_max3_f32 v16, v16, v4, v5
	v_max3_f32 v16, v16, v6, v7
	v_max3_f32 v16, v16, v8, v9
	v_max3_f32 v16, v16, v10, v11
	v_max3_f32 v16, v16, v12, v13
	v_max3_f32 v16, v16, v14, v15
	v_mov_b32_e32 v17, v16
	s_andn2_b64 s[0:1], exec, s[86:87]
	s_andn2_b64 vcc, exec, s[86:87]
	v_permlane32_swap_b32_e32 v16, v17
	s_cbranch_vccnz .LBB0_846
	s_barrier

.LBB0_850:
	v_fma_f32 v0, v0, s33, -v229
	v_exp_f32_e32 v112, v0
	v_fma_f32 v0, v65, s33, -v229
	v_exp_f32_e32 v97, v0
	v_fma_f32 v0, v1, s33, -v229
	v_exp_f32_e32 v113, v0
	v_fma_f32 v0, v66, s33, -v229
	v_exp_f32_e32 v98, v0
	v_fma_f32 v0, v2, s33, -v229
	v_exp_f32_e32 v114, v0
	v_fma_f32 v0, v67, s33, -v229
	v_exp_f32_e32 v99, v0
	v_fma_f32 v0, v3, s33, -v229
	v_exp_f32_e32 v115, v0
	v_fma_f32 v0, v68, s33, -v229
	v_exp_f32_e32 v100, v0
	v_fma_f32 v0, v4, s33, -v229
	v_exp_f32_e32 v116, v0
	v_fma_f32 v0, v69, s33, -v229
	v_exp_f32_e32 v101, v0
	v_fma_f32 v0, v5, s33, -v229
	v_exp_f32_e32 v117, v0
	v_fma_f32 v0, v70, s33, -v229
	v_exp_f32_e32 v102, v0
	v_fma_f32 v0, v6, s33, -v229
	v_exp_f32_e32 v118, v0
	v_fma_f32 v0, v71, s33, -v229
	v_exp_f32_e32 v103, v0
	v_fma_f32 v0, v7, s33, -v229
	v_exp_f32_e32 v119, v0
	v_fma_f32 v0, v72, s33, -v229
	v_exp_f32_e32 v104, v0
	v_fma_f32 v0, v8, s33, -v229
	v_exp_f32_e32 v120, v0
	v_fma_f32 v0, v73, s33, -v229
	v_exp_f32_e32 v105, v0
	v_fma_f32 v0, v9, s33, -v229
	v_exp_f32_e32 v121, v0
	v_fma_f32 v0, v74, s33, -v229
	v_exp_f32_e32 v106, v0
	v_fma_f32 v0, v10, s33, -v229
	v_exp_f32_e32 v122, v0
	v_fma_f32 v0, v75, s33, -v229
	v_exp_f32_e32 v107, v0
	v_fma_f32 v0, v11, s33, -v229
	v_exp_f32_e32 v123, v0
	v_fma_f32 v0, v76, s33, -v229
	v_exp_f32_e32 v108, v0
	v_fma_f32 v0, v12, s33, -v229
	v_exp_f32_e32 v124, v0
	v_fma_f32 v0, v77, s33, -v229
	v_exp_f32_e32 v109, v0
	v_fma_f32 v0, v13, s33, -v229
	v_exp_f32_e32 v125, v0
	v_fma_f32 v0, v78, s33, -v229
	v_exp_f32_e32 v110, v0
	v_fma_f32 v0, v14, s33, -v229
	v_exp_f32_e32 v126, v0
	v_fma_f32 v0, v79, s33, -v229
	v_fma_f32 v64, v64, s33, -v229
	v_exp_f32_e32 v111, v0
	v_fma_f32 v0, v15, s33, -v229
	v_exp_f32_e32 v96, v64
	v_exp_f32_e32 v127, v0
	s_andn2_b64 s[70:71], exec, s[76:77]
	s_andn2_b64 vcc, exec, s[76:77]
	v_cvt_pk_bf16_f32 v12, v96, v97
	v_cvt_pk_bf16_f32 v13, v98, v99
	v_cvt_pk_bf16_f32 v14, v100, v101
	v_cvt_pk_bf16_f32 v15, v102, v103
	v_cvt_pk_bf16_f32 v8, v104, v105
	v_cvt_pk_bf16_f32 v9, v106, v107
	v_cvt_pk_bf16_f32 v10, v108, v109
	v_cvt_pk_bf16_f32 v11, v110, v111
	v_cvt_pk_bf16_f32 v4, v112, v113
	v_cvt_pk_bf16_f32 v5, v114, v115
	v_cvt_pk_bf16_f32 v6, v116, v117
	v_cvt_pk_bf16_f32 v7, v118, v119
	v_cvt_pk_bf16_f32 v0, v120, v121
	v_cvt_pk_bf16_f32 v1, v122, v123
	v_cvt_pk_bf16_f32 v2, v124, v125
	v_cvt_pk_bf16_f32 v3, v126, v127
	s_cbranch_vccnz .LBB0_855
	s_cmp_lt_i32 s2, 0
	s_mov_b64 s[80:81], -1
	s_cbranch_scc0 .LBB0_853
	s_waitcnt vmcnt(0)
	s_mov_b64 s[80:81], 0

.LBB0_1005:
	s_ashr_i32 s4, s44, 31
	s_lshr_b32 s4, s4, 20
	s_add_i32 s4, s44, s4
	s_ashr_i32 s4, s4, 12
	s_mul_hi_i32 s5, s4, 0xc000
	s_mul_i32 s4, s4, 0xc000
	v_lshl_or_b32 v166, s45, 8, v182
	s_add_u32 s4, s38, s4
	s_addc_u32 s5, s39, s5
	v_ashrrev_i32_e32 v167, 31, v166
	v_lshl_add_u64 v[76:77], v[166:167], 2, s[4:5]
	global_load_dwordx4 v[80:83], v[76:77], off offset:16
	global_load_dwordx4 v[84:87], v[76:77], off
	global_load_dwordx4 v[68:71], v[76:77], off offset:528
	s_nop 0
	global_load_dwordx4 v[76:79], v[76:77], off offset:512
	v_add_u32_e32 v172, s44, v180
	v_ashrrev_i32_e32 v173, 31, v172
	v_lshlrev_b64 v[144:145], 11, v[172:173]
	v_lshl_add_u64 v[178:179], v[144:145], 0, v[166:167]
	s_andn2_b64 s[4:5], exec, s[8:9]
	s_andn2_b64 vcc, exec, s[8:9]
	v_lshl_add_u64 v[176:177], v[178:179], 1, s[10:11]
	s_and_b64 vcc, exec, s[8:9]
	s_cbranch_vccz .LO1_f32
	v_mov_b32_e32 v184, v178
	v_mov_b32_e32 v185, v179
	v_mov_b32_e32 v188, v178
	v_mov_b32_e32 v189, v179
	v_lshl_add_u64 v[174:175], v[184:185], 1, s[10:11]
	global_load_dwordx4 v[148:151], v[174:175], off
	global_load_dwordx4 v[212:215], v[174:175], off offset:256
	s_mov_b64 s[98:99], 0x8000
	v_lshl_add_u64 v[184:185], v[184:185], 0, s[98:99]
	v_lshl_add_u64 v[174:175], v[184:185], 1, s[10:11]
	global_load_dwordx4 v[220:223], v[174:175], off
	global_load_dwordx4 v[228:231], v[174:175], off offset:256
	s_mov_b64 s[98:99], 0x8000
	v_lshl_add_u64 v[184:185], v[184:185], 0, s[98:99]
	v_lshl_add_u64 v[174:175], v[184:185], 1, s[10:11]
	global_load_dwordx4 v[236:239], v[174:175], off
	s_waitcnt vmcnt(4)
	v_lshlrev_b32_e32 v144, 16, v148
	v_and_b32_e32 v145, 0xffff0000, v148
	v_lshlrev_b32_e32 v146, 16, v149
	v_and_b32_e32 v147, 0xffff0000, v149
	v_lshlrev_b32_e32 v148, 16, v150
	v_and_b32_e32 v149, 0xffff0000, v150
	v_lshlrev_b32_e32 v150, 16, v151
	v_and_b32_e32 v151, 0xffff0000, v151
	v_pk_fma_f32 v[144:145], v[140:141], v[84:85], v[144:145]
	v_pk_fma_f32 v[146:147], v[142:143], v[86:87], v[146:147]
	v_pk_fma_f32 v[148:149], v[136:137], v[80:81], v[148:149]
	v_pk_fma_f32 v[150:151], v[138:139], v[82:83], v[150:151]
	v_lshl_add_u64 v[176:177], v[188:189], 1, s[12:13]
	v_cvt_pk_bf16_f32 v144, v144, v145
	v_cvt_pk_bf16_f32 v145, v146, v147
	v_cvt_pk_bf16_f32 v146, v148, v149
	v_cvt_pk_bf16_f32 v147, v150, v151
	global_store_dwordx4 v[176:177], v[144:147], off
	global_load_dwordx4 v[244:247], v[174:175], off offset:256
	s_waitcnt vmcnt(5)
	v_lshlrev_b32_e32 v208, 16, v212
	v_and_b32_e32 v209, 0xffff0000, v212
	v_lshlrev_b32_e32 v210, 16, v213
	v_and_b32_e32 v211, 0xffff0000, v213
	v_lshlrev_b32_e32 v212, 16, v214
	v_and_b32_e32 v213, 0xffff0000, v214
	v_lshlrev_b32_e32 v214, 16, v215
	v_and_b32_e32 v215, 0xffff0000, v215
	v_pk_fma_f32 v[208:209], v[132:133], v[76:77], v[208:209]
	v_pk_fma_f32 v[210:211], v[134:135], v[78:79], v[210:211]
	v_pk_fma_f32 v[212:213], v[128:129], v[68:69], v[212:213]
	v_pk_fma_f32 v[214:215], v[130:131], v[70:71], v[214:215]
	v_cvt_pk_bf16_f32 v208, v208, v209
	v_cvt_pk_bf16_f32 v209, v210, v211
	v_cvt_pk_bf16_f32 v210, v212, v213
	v_cvt_pk_bf16_f32 v211, v214, v215
	global_store_dwordx4 v[176:177], v[208:211], off offset:256
	s_mov_b64 s[98:99], 0x8000
	v_lshl_add_u64 v[184:185], v[184:185], 0, s[98:99]
	v_lshl_add_u64 v[174:175], v[184:185], 1, s[10:11]
	global_load_dwordx4 v[148:151], v[174:175], off
	s_waitcnt vmcnt(6)
	v_lshlrev_b32_e32 v216, 16, v220
	v_and_b32_e32 v217, 0xffff0000, v220
	v_lshlrev_b32_e32 v218, 16, v221
	v_and_b32_e32 v219, 0xffff0000, v221
	v_lshlrev_b32_e32 v220, 16, v222
	v_and_b32_e32 v221, 0xffff0000, v222
	v_lshlrev_b32_e32 v222, 16, v223
	v_and_b32_e32 v223, 0xffff0000, v223
	v_pk_fma_f32 v[216:217], v[124:125], v[84:85], v[216:217]
	v_pk_fma_f32 v[218:219], v[126:127], v[86:87], v[218:219]
	v_pk_fma_f32 v[220:221], v[120:121], v[80:81], v[220:221]
	v_pk_fma_f32 v[222:223], v[122:123], v[82:83], v[222:223]
	s_mov_b64 s[98:99], 0x8000
	v_lshl_add_u64 v[188:189], v[188:189], 0, s[98:99]
	v_lshl_add_u64 v[176:177], v[188:189], 1, s[12:13]
	v_cvt_pk_bf16_f32 v216, v216, v217
	v_cvt_pk_bf16_f32 v217, v218, v219
	v_cvt_pk_bf16_f32 v218, v220, v221
	v_cvt_pk_bf16_f32 v219, v222, v223
	global_store_dwordx4 v[176:177], v[216:219], off
	global_load_dwordx4 v[212:215], v[174:175], off offset:256
	s_waitcnt vmcnt(7)
	v_lshlrev_b32_e32 v224, 16, v228
	v_and_b32_e32 v225, 0xffff0000, v228
	v_lshlrev_b32_e32 v226, 16, v229
	v_and_b32_e32 v227, 0xffff0000, v229
	v_lshlrev_b32_e32 v228, 16, v230
	v_and_b32_e32 v229, 0xffff0000, v230
	v_lshlrev_b32_e32 v230, 16, v231
	v_and_b32_e32 v231, 0xffff0000, v231
	v_pk_fma_f32 v[224:225], v[116:117], v[76:77], v[224:225]
	v_pk_fma_f32 v[226:227], v[118:119], v[78:79], v[226:227]
	v_pk_fma_f32 v[228:229], v[112:113], v[68:69], v[228:229]
	v_pk_fma_f32 v[230:231], v[114:115], v[70:71], v[230:231]
	v_cvt_pk_bf16_f32 v224, v224, v225
	v_cvt_pk_bf16_f32 v225, v226, v227
	v_cvt_pk_bf16_f32 v226, v228, v229
	v_cvt_pk_bf16_f32 v227, v230, v231
	global_store_dwordx4 v[176:177], v[224:227], off offset:256
	s_mov_b64 s[98:99], 0x28000
	v_lshl_add_u64 v[184:185], v[184:185], 0, s[98:99]
	v_lshl_add_u64 v[174:175], v[184:185], 1, s[10:11]
	global_load_dwordx4 v[220:223], v[174:175], off
	s_waitcnt vmcnt(8)
	v_lshlrev_b32_e32 v232, 16, v236
	v_and_b32_e32 v233, 0xffff0000, v236
	v_lshlrev_b32_e32 v234, 16, v237
	v_and_b32_e32 v235, 0xffff0000, v237
	v_lshlrev_b32_e32 v236, 16, v238
	v_and_b32_e32 v237, 0xffff0000, v238
	v_lshlrev_b32_e32 v238, 16, v239
	v_and_b32_e32 v239, 0xffff0000, v239
	v_pk_fma_f32 v[232:233], v[108:109], v[84:85], v[232:233]
	v_pk_fma_f32 v[234:235], v[110:111], v[86:87], v[234:235]
	v_pk_fma_f32 v[236:237], v[104:105], v[80:81], v[236:237]
	v_pk_fma_f32 v[238:239], v[106:107], v[82:83], v[238:239]
	s_mov_b64 s[98:99], 0x8000
	v_lshl_add_u64 v[188:189], v[188:189], 0, s[98:99]
	v_lshl_add_u64 v[176:177], v[188:189], 1, s[12:13]
	v_cvt_pk_bf16_f32 v232, v232, v233
	v_cvt_pk_bf16_f32 v233, v234, v235
	v_cvt_pk_bf16_f32 v234, v236, v237
	v_cvt_pk_bf16_f32 v235, v238, v239
	global_store_dwordx4 v[176:177], v[232:235], off
	global_load_dwordx4 v[228:231], v[174:175], off offset:256
	s_waitcnt vmcnt(8)
	v_lshlrev_b32_e32 v240, 16, v244
	v_and_b32_e32 v241, 0xffff0000, v244
	v_lshlrev_b32_e32 v242, 16, v245
	v_and_b32_e32 v243, 0xffff0000, v245
	v_lshlrev_b32_e32 v244, 16, v246
	v_and_b32_e32 v245, 0xffff0000, v246
	v_lshlrev_b32_e32 v246, 16, v247
	v_and_b32_e32 v247, 0xffff0000, v247
	v_pk_fma_f32 v[240:241], v[100:101], v[76:77], v[240:241]
	v_pk_fma_f32 v[242:243], v[102:103], v[78:79], v[242:243]
	v_pk_fma_f32 v[244:245], v[96:97], v[68:69], v[244:245]
	v_pk_fma_f32 v[246:247], v[98:99], v[70:71], v[246:247]
	v_cvt_pk_bf16_f32 v240, v240, v241
	v_cvt_pk_bf16_f32 v241, v242, v243
	v_cvt_pk_bf16_f32 v242, v244, v245
	v_cvt_pk_bf16_f32 v243, v246, v247
	global_store_dwordx4 v[176:177], v[240:243], off offset:256
	s_mov_b64 s[98:99], 0x8000
	v_lshl_add_u64 v[184:185], v[184:185], 0, s[98:99]
	v_lshl_add_u64 v[174:175], v[184:185], 1, s[10:11]
	global_load_dwordx4 v[236:239], v[174:175], off
	s_waitcnt vmcnt(8)
	v_lshlrev_b32_e32 v144, 16, v148
	v_and_b32_e32 v145, 0xffff0000, v148
	v_lshlrev_b32_e32 v146, 16, v149
	v_and_b32_e32 v147, 0xffff0000, v149
	v_lshlrev_b32_e32 v148, 16, v150
	v_and_b32_e32 v149, 0xffff0000, v150
	v_lshlrev_b32_e32 v150, 16, v151
	v_and_b32_e32 v151, 0xffff0000, v151
	v_pk_fma_f32 v[144:145], v[92:93], v[84:85], v[144:145]
	v_pk_fma_f32 v[146:147], v[94:95], v[86:87], v[146:147]
	v_pk_fma_f32 v[148:149], v[88:89], v[80:81], v[148:149]
	v_pk_fma_f32 v[150:151], v[90:91], v[82:83], v[150:151]
	s_mov_b64 s[98:99], 0x8000
	v_lshl_add_u64 v[188:189], v[188:189], 0, s[98:99]
	v_lshl_add_u64 v[176:177], v[188:189], 1, s[12:13]
	v_cvt_pk_bf16_f32 v144, v144, v145
	v_cvt_pk_bf16_f32 v145, v146, v147
	v_cvt_pk_bf16_f32 v146, v148, v149
	v_cvt_pk_bf16_f32 v147, v150, v151
	global_store_dwordx4 v[176:177], v[144:147], off
	global_load_dwordx4 v[244:247], v[174:175], off offset:256
	s_waitcnt vmcnt(8)
	v_lshlrev_b32_e32 v208, 16, v212
	v_and_b32_e32 v209, 0xffff0000, v212
	v_lshlrev_b32_e32 v210, 16, v213
	v_and_b32_e32 v211, 0xffff0000, v213
	v_lshlrev_b32_e32 v212, 16, v214
	v_and_b32_e32 v213, 0xffff0000, v214
	v_lshlrev_b32_e32 v214, 16, v215
	v_and_b32_e32 v215, 0xffff0000, v215
	v_pk_fma_f32 v[208:209], v[72:73], v[76:77], v[208:209]
	v_pk_fma_f32 v[210:211], v[74:75], v[78:79], v[210:211]
	v_pk_fma_f32 v[212:213], v[64:65], v[68:69], v[212:213]
	v_pk_fma_f32 v[214:215], v[66:67], v[70:71], v[214:215]
	v_cvt_pk_bf16_f32 v208, v208, v209
	v_cvt_pk_bf16_f32 v209, v210, v211
	v_cvt_pk_bf16_f32 v210, v212, v213
	v_cvt_pk_bf16_f32 v211, v214, v215
	global_store_dwordx4 v[176:177], v[208:211], off offset:256
	s_mov_b64 s[98:99], 0x8000
	v_lshl_add_u64 v[184:185], v[184:185], 0, s[98:99]
	v_lshl_add_u64 v[174:175], v[184:185], 1, s[10:11]
	global_load_dwordx4 v[148:151], v[174:175], off
	s_waitcnt vmcnt(8)
	v_lshlrev_b32_e32 v216, 16, v220
	v_and_b32_e32 v217, 0xffff0000, v220
	v_lshlrev_b32_e32 v218, 16, v221
	v_and_b32_e32 v219, 0xffff0000, v221
	v_lshlrev_b32_e32 v220, 16, v222
	v_and_b32_e32 v221, 0xffff0000, v222
	v_lshlrev_b32_e32 v222, 16, v223
	v_and_b32_e32 v223, 0xffff0000, v223
	v_pk_fma_f32 v[216:217], v[60:61], v[84:85], v[216:217]
	v_pk_fma_f32 v[218:219], v[62:63], v[86:87], v[218:219]
	v_pk_fma_f32 v[220:221], v[56:57], v[80:81], v[220:221]
	v_pk_fma_f32 v[222:223], v[58:59], v[82:83], v[222:223]
	s_mov_b64 s[98:99], 0x28000
	v_lshl_add_u64 v[188:189], v[188:189], 0, s[98:99]
	v_lshl_add_u64 v[176:177], v[188:189], 1, s[12:13]
	v_cvt_pk_bf16_f32 v216, v216, v217
	v_cvt_pk_bf16_f32 v217, v218, v219
	v_cvt_pk_bf16_f32 v218, v220, v221
	v_cvt_pk_bf16_f32 v219, v222, v223
	global_store_dwordx4 v[176:177], v[216:219], off
	global_load_dwordx4 v[212:215], v[174:175], off offset:256
	s_waitcnt vmcnt(8)
	v_lshlrev_b32_e32 v224, 16, v228
	v_and_b32_e32 v225, 0xffff0000, v228
	v_lshlrev_b32_e32 v226, 16, v229
	v_and_b32_e32 v227, 0xffff0000, v229
	v_lshlrev_b32_e32 v228, 16, v230
	v_and_b32_e32 v229, 0xffff0000, v230
	v_lshlrev_b32_e32 v230, 16, v231
	v_and_b32_e32 v231, 0xffff0000, v231
	v_pk_fma_f32 v[224:225], v[52:53], v[76:77], v[224:225]
	v_pk_fma_f32 v[226:227], v[54:55], v[78:79], v[226:227]
	v_pk_fma_f32 v[228:229], v[48:49], v[68:69], v[228:229]
	v_pk_fma_f32 v[230:231], v[50:51], v[70:71], v[230:231]
	v_cvt_pk_bf16_f32 v224, v224, v225
	v_cvt_pk_bf16_f32 v225, v226, v227
	v_cvt_pk_bf16_f32 v226, v228, v229
	v_cvt_pk_bf16_f32 v227, v230, v231
	global_store_dwordx4 v[176:177], v[224:227], off offset:256
	s_mov_b64 s[98:99], 0x8000
	v_lshl_add_u64 v[184:185], v[184:185], 0, s[98:99]
	v_lshl_add_u64 v[174:175], v[184:185], 1, s[10:11]
	global_load_dwordx4 v[220:223], v[174:175], off
	s_waitcnt vmcnt(8)
	v_lshlrev_b32_e32 v232, 16, v236
	v_and_b32_e32 v233, 0xffff0000, v236
	v_lshlrev_b32_e32 v234, 16, v237
	v_and_b32_e32 v235, 0xffff0000, v237
	v_lshlrev_b32_e32 v236, 16, v238
	v_and_b32_e32 v237, 0xffff0000, v238
	v_lshlrev_b32_e32 v238, 16, v239
	v_and_b32_e32 v239, 0xffff0000, v239
	v_pk_fma_f32 v[232:233], v[44:45], v[84:85], v[232:233]
	v_pk_fma_f32 v[234:235], v[46:47], v[86:87], v[234:235]
	v_pk_fma_f32 v[236:237], v[40:41], v[80:81], v[236:237]
	v_pk_fma_f32 v[238:239], v[42:43], v[82:83], v[238:239]
	s_mov_b64 s[98:99], 0x8000
	v_lshl_add_u64 v[188:189], v[188:189], 0, s[98:99]
	v_lshl_add_u64 v[176:177], v[188:189], 1, s[12:13]
	v_cvt_pk_bf16_f32 v232, v232, v233
	v_cvt_pk_bf16_f32 v233, v234, v235
	v_cvt_pk_bf16_f32 v234, v236, v237
	v_cvt_pk_bf16_f32 v235, v238, v239
	global_store_dwordx4 v[176:177], v[232:235], off
	global_load_dwordx4 v[228:231], v[174:175], off offset:256
	s_waitcnt vmcnt(8)
	v_lshlrev_b32_e32 v240, 16, v244
	v_and_b32_e32 v241, 0xffff0000, v244
	v_lshlrev_b32_e32 v242, 16, v245
	v_and_b32_e32 v243, 0xffff0000, v245
	v_lshlrev_b32_e32 v244, 16, v246
	v_and_b32_e32 v245, 0xffff0000, v246
	v_lshlrev_b32_e32 v246, 16, v247
	v_and_b32_e32 v247, 0xffff0000, v247
	v_pk_fma_f32 v[240:241], v[36:37], v[76:77], v[240:241]
	v_pk_fma_f32 v[242:243], v[38:39], v[78:79], v[242:243]
	v_pk_fma_f32 v[244:245], v[32:33], v[68:69], v[244:245]
	v_pk_fma_f32 v[246:247], v[34:35], v[70:71], v[246:247]
	v_cvt_pk_bf16_f32 v240, v240, v241
	v_cvt_pk_bf16_f32 v241, v242, v243
	v_cvt_pk_bf16_f32 v242, v244, v245
	v_cvt_pk_bf16_f32 v243, v246, v247
	global_store_dwordx4 v[176:177], v[240:243], off offset:256
	s_waitcnt vmcnt(7)
	v_lshlrev_b32_e32 v144, 16, v148
	v_and_b32_e32 v145, 0xffff0000, v148
	v_lshlrev_b32_e32 v146, 16, v149
	v_and_b32_e32 v147, 0xffff0000, v149
	v_lshlrev_b32_e32 v148, 16, v150
	v_and_b32_e32 v149, 0xffff0000, v150
	v_lshlrev_b32_e32 v150, 16, v151
	v_and_b32_e32 v151, 0xffff0000, v151
	v_pk_fma_f32 v[144:145], v[28:29], v[84:85], v[144:145]
	v_pk_fma_f32 v[146:147], v[30:31], v[86:87], v[146:147]
	v_pk_fma_f32 v[148:149], v[20:21], v[80:81], v[148:149]
	v_pk_fma_f32 v[150:151], v[22:23], v[82:83], v[150:151]
	s_mov_b64 s[98:99], 0x8000
	v_lshl_add_u64 v[188:189], v[188:189], 0, s[98:99]
	v_lshl_add_u64 v[176:177], v[188:189], 1, s[12:13]
	v_cvt_pk_bf16_f32 v144, v144, v145
	v_cvt_pk_bf16_f32 v145, v146, v147
	v_cvt_pk_bf16_f32 v146, v148, v149
	v_cvt_pk_bf16_f32 v147, v150, v151
	global_store_dwordx4 v[176:177], v[144:147], off
	s_waitcnt vmcnt(6)
	v_lshlrev_b32_e32 v208, 16, v212
	v_and_b32_e32 v209, 0xffff0000, v212
	v_lshlrev_b32_e32 v210, 16, v213
	v_and_b32_e32 v211, 0xffff0000, v213
	v_lshlrev_b32_e32 v212, 16, v214
	v_and_b32_e32 v213, 0xffff0000, v214
	v_lshlrev_b32_e32 v214, 16, v215
	v_and_b32_e32 v215, 0xffff0000, v215
	v_pk_fma_f32 v[208:209], v[24:25], v[76:77], v[208:209]
	v_pk_fma_f32 v[210:211], v[26:27], v[78:79], v[210:211]
	v_pk_fma_f32 v[212:213], v[16:17], v[68:69], v[212:213]
	v_pk_fma_f32 v[214:215], v[18:19], v[70:71], v[214:215]
	v_cvt_pk_bf16_f32 v208, v208, v209
	v_cvt_pk_bf16_f32 v209, v210, v211
	v_cvt_pk_bf16_f32 v210, v212, v213
	v_cvt_pk_bf16_f32 v211, v214, v215
	global_store_dwordx4 v[176:177], v[208:211], off offset:256
	s_waitcnt vmcnt(5)
	v_lshlrev_b32_e32 v216, 16, v220
	v_and_b32_e32 v217, 0xffff0000, v220
	v_lshlrev_b32_e32 v218, 16, v221
	v_and_b32_e32 v219, 0xffff0000, v221
	v_lshlrev_b32_e32 v220, 16, v222
	v_and_b32_e32 v221, 0xffff0000, v222
	v_lshlrev_b32_e32 v222, 16, v223
	v_and_b32_e32 v223, 0xffff0000, v223
	v_pk_fma_f32 v[216:217], v[8:9], v[84:85], v[216:217]
	v_pk_fma_f32 v[218:219], v[10:11], v[86:87], v[218:219]
	v_pk_fma_f32 v[220:221], v[0:1], v[80:81], v[220:221]
	v_pk_fma_f32 v[222:223], v[2:3], v[82:83], v[222:223]
	s_mov_b64 s[98:99], 0x8000
	v_lshl_add_u64 v[188:189], v[188:189], 0, s[98:99]
	v_lshl_add_u64 v[176:177], v[188:189], 1, s[12:13]
	v_cvt_pk_bf16_f32 v216, v216, v217
	v_cvt_pk_bf16_f32 v217, v218, v219
	v_cvt_pk_bf16_f32 v218, v220, v221
	v_cvt_pk_bf16_f32 v219, v222, v223
	global_store_dwordx4 v[176:177], v[216:219], off
	s_waitcnt vmcnt(4)
	v_lshlrev_b32_e32 v224, 16, v228
	v_and_b32_e32 v225, 0xffff0000, v228
	v_lshlrev_b32_e32 v226, 16, v229
	v_and_b32_e32 v227, 0xffff0000, v229
	v_lshlrev_b32_e32 v228, 16, v230
	v_and_b32_e32 v229, 0xffff0000, v230
	v_lshlrev_b32_e32 v230, 16, v231
	v_and_b32_e32 v231, 0xffff0000, v231
	v_pk_fma_f32 v[224:225], v[12:13], v[76:77], v[224:225]
	v_pk_fma_f32 v[226:227], v[14:15], v[78:79], v[226:227]
	v_pk_fma_f32 v[228:229], v[4:5], v[68:69], v[228:229]
	v_pk_fma_f32 v[230:231], v[6:7], v[70:71], v[230:231]
	v_cvt_pk_bf16_f32 v224, v224, v225
	v_cvt_pk_bf16_f32 v225, v226, v227
	v_cvt_pk_bf16_f32 v226, v228, v229
	v_cvt_pk_bf16_f32 v227, v230, v231
	global_store_dwordx4 v[176:177], v[224:227], off offset:256
	s_branch .LO1_done

.LBB0_1375:
	v_add_u32_e32 v5, 0x2000, v5
	v_ashrrev_i32_e32 v6, 31, v5
	v_lshrrev_b32_e32 v6, 22, v6
	v_add_u32_e32 v6, v5, v6
	v_ashrrev_i32_e32 v6, 10, v6
	v_mul_i32_i24_e32 v7, 0x400, v6
	v_sub_u32_e32 v5, v5, v7
	v_lshrrev_b32_e32 v7, 4, v5
	v_bitop3_b32 v7, v7, v5, 32 bitop3:0x6c
	v_lshlrev_b32_e32 v5, 3, v6
	v_and_b32_e32 v8, -16, v5
	v_ashrrev_i32_e32 v5, 31, v7
	v_lshrrev_b32_e32 v5, 26, v5
	v_add_u32_e32 v5, v7, v5
	v_ashrrev_i32_e32 v5, 6, v5
	v_add_u32_e32 v147, v5, v8
	s_andn2_b64 s[0:1], exec, s[4:5]
	s_andn2_b64 vcc, exec, s[4:5]
	s_mov_b64 s[4:5], -1
	s_cbranch_vccnz .LBB0_1377
	v_add_u32_e32 v8, s9, v147
	s_cbranch_execnz .LBB0_1379
	s_branch .LBB0_1378
